# grid barrier: arrive atomic issued first, LDS generation read under it, invalidate moved after the release decision
# baseline (speedup 1.0000x reference)
.LBB0_230:
	v_writelane_b32 v253, s40, 46
	s_cmp_gt_i32 s81, 1
	s_cselect_b64 s[4:5], -1, 0
	v_writelane_b32 v253, s41, 47
	v_writelane_b32 v253, s42, 48
	v_writelane_b32 v253, s43, 49
	v_writelane_b32 v253, s44, 50
	v_writelane_b32 v253, s45, 51
	v_writelane_b32 v253, s46, 52
	v_writelane_b32 v253, s47, 53
	v_writelane_b32 v253, s48, 54
	v_writelane_b32 v253, s49, 55
	v_writelane_b32 v253, s50, 56
	v_writelane_b32 v253, s51, 57
	v_writelane_b32 v253, s52, 58
	v_writelane_b32 v253, s53, 59
	s_and_b64 s[0:1], s[0:1], s[4:5]
	v_writelane_b32 v253, s54, 60
	s_andn2_b64 vcc, exec, s[0:1]
	v_writelane_b32 v253, s55, 61
	s_cbranch_vccnz .LBB0_284
	s_waitcnt vmcnt(0)
	s_barrier
	s_and_saveexec_b64 s[0:1], s[78:79]
	s_cbranch_execz .LBB0_283
	v_mov_b32_e32 v3, 1
	v_mov_b32_e32 v4, s99
	v_and_b32_e32 v5, 0xffff, v4
	v_mov_b32_e32 v1, 0x22160
	global_atomic_add v7, v5, v3, s[100:101] sc0
	ds_read_b32 v2, v1
	v_lshrrev_b32_e32 v6, 16, v4
	v_lshrrev_b32_e32 v8, 8, v5
	v_sub_u32_e32 v8, s98, v8
	v_add_u32_e32 v8, 7, v8
	v_lshrrev_b32_e32 v8, 3, v8
	v_mov_b32_e32 v9, s98
	v_min_u32_e32 v9, 8, v9
	v_mov_b32_e32 v10, 0
	s_waitcnt lgkmcnt(0)
	v_add_u32_e32 v2, 1, v2
	ds_write_b32 v1, v2
	v_mul_lo_u32 v8, v8, v2
	v_mul_lo_u32 v9, v9, v2
	s_waitcnt vmcnt(0)
	v_add_u32_e32 v7, 1, v7
	v_cmp_eq_u32_e32 vcc, v7, v8
	s_cbranch_vccz .Lgb_poll_0
	v_mov_b32_e32 v4, 0
	global_atomic_add v4, v3, s[100:101] offset:2048
	global_atomic_add v4, v3, s[100:101] offset:2304
	global_atomic_add v4, v3, s[100:101] offset:2560
	global_atomic_add v4, v3, s[100:101] offset:2816
	global_atomic_add v4, v3, s[100:101] offset:3072
	global_atomic_add v4, v3, s[100:101] offset:3328
	global_atomic_add v4, v3, s[100:101] offset:3584
	global_atomic_add v4, v3, s[100:101] offset:3840
.Lgb_poll_0:
	buffer_inv sc1
.Lgb_spin_0:
	global_load_dword v11, v6, s[100:101] sc1
	v_add_u32_e32 v10, 1, v10
	s_waitcnt vmcnt(0)
	v_cmp_ge_u32_e32 vcc, v11, v9
	s_cbranch_vccnz .Lgb_done_0
	v_cmp_gt_u32_e32 vcc, 0x80000, v10
	s_sleep 1
	s_cbranch_vccnz .Lgb_spin_0

.LBB0_306:
	s_cmp_gt_i32 s81, 2
	s_cselect_b64 s[4:5], -1, 0
	s_and_b64 s[0:1], s[0:1], s[4:5]
	s_andn2_b64 vcc, exec, s[0:1]
	s_cbranch_vccnz .LBB0_360
	s_waitcnt vmcnt(0)
	s_waitcnt vmcnt(0)
	s_barrier
	s_and_saveexec_b64 s[0:1], s[78:79]
	s_cbranch_execz .LBB0_359
	v_mov_b32_e32 v3, 1
	v_mov_b32_e32 v4, s99
	v_and_b32_e32 v5, 0xffff, v4
	v_mov_b32_e32 v1, 0x22160
	global_atomic_add v7, v5, v3, s[100:101] sc0
	ds_read_b32 v2, v1
	v_lshrrev_b32_e32 v6, 16, v4
	v_lshrrev_b32_e32 v8, 8, v5
	v_sub_u32_e32 v8, s98, v8
	v_add_u32_e32 v8, 7, v8
	v_lshrrev_b32_e32 v8, 3, v8
	v_mov_b32_e32 v9, s98
	v_min_u32_e32 v9, 8, v9
	v_mov_b32_e32 v10, 0
	s_waitcnt lgkmcnt(0)
	v_add_u32_e32 v2, 1, v2
	ds_write_b32 v1, v2
	v_mul_lo_u32 v8, v8, v2
	v_mul_lo_u32 v9, v9, v2
	s_waitcnt vmcnt(0)
	v_add_u32_e32 v7, 1, v7
	v_cmp_eq_u32_e32 vcc, v7, v8
	s_cbranch_vccz .Lgb_poll_1
	v_mov_b32_e32 v4, 0
	global_atomic_add v4, v3, s[100:101] offset:2048
	global_atomic_add v4, v3, s[100:101] offset:2304
	global_atomic_add v4, v3, s[100:101] offset:2560
	global_atomic_add v4, v3, s[100:101] offset:2816
	global_atomic_add v4, v3, s[100:101] offset:3072
	global_atomic_add v4, v3, s[100:101] offset:3328
	global_atomic_add v4, v3, s[100:101] offset:3584
	global_atomic_add v4, v3, s[100:101] offset:3840
.Lgb_poll_1:
	buffer_inv sc1
.Lgb_spin_1:
	global_load_dword v11, v6, s[100:101] sc1
	v_add_u32_e32 v10, 1, v10
	s_waitcnt vmcnt(0)
	v_cmp_ge_u32_e32 vcc, v11, v9
	s_cbranch_vccnz .Lgb_done_1
	v_cmp_gt_u32_e32 vcc, 0x80000, v10
	s_sleep 1
	s_cbranch_vccnz .Lgb_spin_1

.LBB0_427:
	s_cmp_gt_i32 s81, 3
	s_cselect_b64 s[4:5], -1, 0
	s_and_b64 s[6:7], s[36:37], s[4:5]
	s_andn2_b64 vcc, exec, s[6:7]
	s_cbranch_vccnz .LBB0_481
	s_waitcnt vmcnt(0)
	s_waitcnt vmcnt(0)
	s_barrier
	s_and_saveexec_b64 s[6:7], s[78:79]
	s_cbranch_execz .LBB0_480
	v_mov_b32_e32 v3, 1
	v_mov_b32_e32 v4, s99
	v_and_b32_e32 v5, 0xffff, v4
	v_mov_b32_e32 v1, 0x22160
	global_atomic_add v7, v5, v3, s[100:101] sc0
	ds_read_b32 v2, v1
	v_lshrrev_b32_e32 v6, 16, v4
	v_lshrrev_b32_e32 v8, 8, v5
	v_sub_u32_e32 v8, s98, v8
	v_add_u32_e32 v8, 7, v8
	v_lshrrev_b32_e32 v8, 3, v8
	v_mov_b32_e32 v9, s98
	v_min_u32_e32 v9, 8, v9
	v_mov_b32_e32 v10, 0
	s_waitcnt lgkmcnt(0)
	v_add_u32_e32 v2, 1, v2
	ds_write_b32 v1, v2
	v_mul_lo_u32 v8, v8, v2
	v_mul_lo_u32 v9, v9, v2
	s_waitcnt vmcnt(0)
	v_add_u32_e32 v7, 1, v7
	v_cmp_eq_u32_e32 vcc, v7, v8
	s_cbranch_vccz .Lgb_poll_2
	v_mov_b32_e32 v4, 0
	global_atomic_add v4, v3, s[100:101] offset:2048
	global_atomic_add v4, v3, s[100:101] offset:2304
	global_atomic_add v4, v3, s[100:101] offset:2560
	global_atomic_add v4, v3, s[100:101] offset:2816
	global_atomic_add v4, v3, s[100:101] offset:3072
	global_atomic_add v4, v3, s[100:101] offset:3328
	global_atomic_add v4, v3, s[100:101] offset:3584
	global_atomic_add v4, v3, s[100:101] offset:3840
.Lgb_poll_2:
	buffer_inv sc1
.Lgb_spin_2:
	global_load_dword v11, v6, s[100:101] sc1
	v_add_u32_e32 v10, 1, v10
	s_waitcnt vmcnt(0)
	v_cmp_ge_u32_e32 vcc, v11, v9
	s_cbranch_vccnz .Lgb_done_2
	v_cmp_gt_u32_e32 vcc, 0x80000, v10
	s_sleep 1
	s_cbranch_vccnz .Lgb_spin_2

.LBB0_601:
	s_andn2_b64 vcc, exec, s[10:11]
	s_mov_b32 s46, s9
	s_cbranch_vccnz .LBB0_655
	s_waitcnt vmcnt(0)
	s_barrier
	s_mov_b64 s[10:11], exec
	v_readlane_b32 s44, v254, 12
	v_readlane_b32 s45, v254, 13
	s_and_b64 s[44:45], s[10:11], s[44:45]
	s_mov_b64 exec, s[44:45]
	s_cbranch_execz .LBB0_654
	v_mov_b32_e32 v9, 1
	v_mov_b32_e32 v10, s99
	v_and_b32_e32 v11, 0xffff, v10
	v_mov_b32_e32 v7, 0x22160
	global_atomic_add v13, v11, v9, s[100:101] sc0
	ds_read_b32 v8, v7
	v_lshrrev_b32_e32 v12, 16, v10
	v_lshrrev_b32_e32 v14, 8, v11
	v_sub_u32_e32 v14, s98, v14
	v_add_u32_e32 v14, 7, v14
	v_lshrrev_b32_e32 v14, 3, v14
	v_mov_b32_e32 v15, s98
	v_min_u32_e32 v15, 8, v15
	v_mov_b32_e32 v16, 0
	s_waitcnt lgkmcnt(0)
	v_add_u32_e32 v8, 1, v8
	ds_write_b32 v7, v8
	v_mul_lo_u32 v14, v14, v8
	v_mul_lo_u32 v15, v15, v8
	s_waitcnt vmcnt(0)
	v_add_u32_e32 v13, 1, v13
	v_cmp_eq_u32_e32 vcc, v13, v14
	s_cbranch_vccz .Lgb_poll_3
	v_mov_b32_e32 v10, 0
	global_atomic_add v10, v9, s[100:101] offset:2048
	global_atomic_add v10, v9, s[100:101] offset:2304
	global_atomic_add v10, v9, s[100:101] offset:2560
	global_atomic_add v10, v9, s[100:101] offset:2816
	global_atomic_add v10, v9, s[100:101] offset:3072
	global_atomic_add v10, v9, s[100:101] offset:3328
	global_atomic_add v10, v9, s[100:101] offset:3584
	global_atomic_add v10, v9, s[100:101] offset:3840
.Lgb_poll_3:
	buffer_inv sc1
.Lgb_spin_3:
	global_load_dword v17, v12, s[100:101] sc1
	v_add_u32_e32 v16, 1, v16
	s_waitcnt vmcnt(0)
	v_cmp_ge_u32_e32 vcc, v17, v15
	s_cbranch_vccnz .Lgb_done_3
	v_cmp_gt_u32_e32 vcc, 0x80000, v16
	s_sleep 1
	s_cbranch_vccnz .Lgb_spin_3

.LBB0_759:
	s_cmp_gt_i32 s81, 4
	s_cselect_b64 s[0:1], -1, 0
	s_and_b64 s[4:5], s[4:5], s[0:1]
	s_andn2_b64 vcc, exec, s[4:5]
	s_cbranch_vccnz .LBB0_813
	s_waitcnt vmcnt(0)
	s_waitcnt vmcnt(0)
	s_barrier
	s_and_saveexec_b64 s[4:5], s[78:79]
	s_cbranch_execz .LBB0_812
	v_mov_b32_e32 v3, 1
	v_mov_b32_e32 v4, s99
	v_and_b32_e32 v5, 0xffff, v4
	v_mov_b32_e32 v1, 0x22160
	global_atomic_add v7, v5, v3, s[100:101] sc0
	ds_read_b32 v2, v1
	v_lshrrev_b32_e32 v6, 16, v4
	v_lshrrev_b32_e32 v8, 8, v5
	v_sub_u32_e32 v8, s98, v8
	v_add_u32_e32 v8, 7, v8
	v_lshrrev_b32_e32 v8, 3, v8
	v_mov_b32_e32 v9, s98
	v_min_u32_e32 v9, 8, v9
	v_mov_b32_e32 v10, 0
	s_waitcnt lgkmcnt(0)
	v_add_u32_e32 v2, 1, v2
	ds_write_b32 v1, v2
	v_mul_lo_u32 v8, v8, v2
	v_mul_lo_u32 v9, v9, v2
	s_waitcnt vmcnt(0)
	v_add_u32_e32 v7, 1, v7
	v_cmp_eq_u32_e32 vcc, v7, v8
	s_cbranch_vccz .Lgb_poll_4
	v_mov_b32_e32 v4, 0
	global_atomic_add v4, v3, s[100:101] offset:2048
	global_atomic_add v4, v3, s[100:101] offset:2304
	global_atomic_add v4, v3, s[100:101] offset:2560
	global_atomic_add v4, v3, s[100:101] offset:2816
	global_atomic_add v4, v3, s[100:101] offset:3072
	global_atomic_add v4, v3, s[100:101] offset:3328
	global_atomic_add v4, v3, s[100:101] offset:3584
	global_atomic_add v4, v3, s[100:101] offset:3840
.Lgb_poll_4:
	buffer_inv sc1
.Lgb_spin_4:
	global_load_dword v11, v6, s[100:101] sc1
	v_add_u32_e32 v10, 1, v10
	s_waitcnt vmcnt(0)
	v_cmp_ge_u32_e32 vcc, v11, v9
	s_cbranch_vccnz .Lgb_done_4
	v_cmp_gt_u32_e32 vcc, 0x80000, v10
	s_sleep 1
	s_cbranch_vccnz .Lgb_spin_4

.LBB0_843:
	s_cmp_gt_i32 s81, 5
	s_cselect_b64 s[4:5], -1, 0
	s_and_b64 s[0:1], s[0:1], s[4:5]
	s_andn2_b64 vcc, exec, s[0:1]
	s_cbranch_vccnz .LBB0_897
	s_waitcnt vmcnt(0)
	s_waitcnt vmcnt(0)
	s_barrier
	s_and_saveexec_b64 s[0:1], s[78:79]
	s_cbranch_execz .LBB0_896
	v_mov_b32_e32 v3, 1
	v_mov_b32_e32 v4, s99
	v_and_b32_e32 v5, 0xffff, v4
	v_mov_b32_e32 v1, 0x22160
	global_atomic_add v7, v5, v3, s[100:101] sc0
	ds_read_b32 v2, v1
	v_lshrrev_b32_e32 v6, 16, v4
	v_lshrrev_b32_e32 v8, 8, v5
	v_sub_u32_e32 v8, s98, v8
	v_add_u32_e32 v8, 7, v8
	v_lshrrev_b32_e32 v8, 3, v8
	v_mov_b32_e32 v9, s98
	v_min_u32_e32 v9, 8, v9
	v_mov_b32_e32 v10, 0
	s_waitcnt lgkmcnt(0)
	v_add_u32_e32 v2, 1, v2
	ds_write_b32 v1, v2
	v_mul_lo_u32 v8, v8, v2
	v_mul_lo_u32 v9, v9, v2
	s_waitcnt vmcnt(0)
	v_add_u32_e32 v7, 1, v7
	v_cmp_eq_u32_e32 vcc, v7, v8
	s_cbranch_vccz .Lgb_poll_5
	v_mov_b32_e32 v4, 0
	global_atomic_add v4, v3, s[100:101] offset:2048
	global_atomic_add v4, v3, s[100:101] offset:2304
	global_atomic_add v4, v3, s[100:101] offset:2560
	global_atomic_add v4, v3, s[100:101] offset:2816
	global_atomic_add v4, v3, s[100:101] offset:3072
	global_atomic_add v4, v3, s[100:101] offset:3328
	global_atomic_add v4, v3, s[100:101] offset:3584
	global_atomic_add v4, v3, s[100:101] offset:3840
.Lgb_poll_5:
	buffer_inv sc1
.Lgb_spin_5:
	global_load_dword v11, v6, s[100:101] sc1
	v_add_u32_e32 v10, 1, v10
	s_waitcnt vmcnt(0)
	v_cmp_ge_u32_e32 vcc, v11, v9
	s_cbranch_vccnz .Lgb_done_5
	v_cmp_gt_u32_e32 vcc, 0x80000, v10
	s_sleep 1
	s_cbranch_vccnz .Lgb_spin_5

.LBB0_944:
	s_cmp_gt_i32 s81, 6
	s_cselect_b64 s[4:5], -1, 0
	s_and_b64 s[0:1], s[0:1], s[4:5]
	s_andn2_b64 vcc, exec, s[0:1]
	s_cbranch_vccnz .LBB0_998
	s_waitcnt vmcnt(0)
	s_waitcnt vmcnt(0)
	s_barrier
	s_and_saveexec_b64 s[0:1], s[78:79]
	s_cbranch_execz .LBB0_997
	v_mov_b32_e32 v3, 1
	v_mov_b32_e32 v4, s99
	v_and_b32_e32 v5, 0xffff, v4
	v_mov_b32_e32 v1, 0x22160
	global_atomic_add v7, v5, v3, s[100:101] sc0
	ds_read_b32 v2, v1
	v_lshrrev_b32_e32 v6, 16, v4
	v_lshrrev_b32_e32 v8, 8, v5
	v_sub_u32_e32 v8, s98, v8
	v_add_u32_e32 v8, 7, v8
	v_lshrrev_b32_e32 v8, 3, v8
	v_mov_b32_e32 v9, s98
	v_min_u32_e32 v9, 8, v9
	v_mov_b32_e32 v10, 0
	s_waitcnt lgkmcnt(0)
	v_add_u32_e32 v2, 1, v2
	ds_write_b32 v1, v2
	v_mul_lo_u32 v8, v8, v2
	v_mul_lo_u32 v9, v9, v2
	s_waitcnt vmcnt(0)
	v_add_u32_e32 v7, 1, v7
	v_cmp_eq_u32_e32 vcc, v7, v8
	s_cbranch_vccz .Lgb_poll_6
	v_mov_b32_e32 v4, 0
	global_atomic_add v4, v3, s[100:101] offset:2048
	global_atomic_add v4, v3, s[100:101] offset:2304
	global_atomic_add v4, v3, s[100:101] offset:2560
	global_atomic_add v4, v3, s[100:101] offset:2816
	global_atomic_add v4, v3, s[100:101] offset:3072
	global_atomic_add v4, v3, s[100:101] offset:3328
	global_atomic_add v4, v3, s[100:101] offset:3584
	global_atomic_add v4, v3, s[100:101] offset:3840
.Lgb_poll_6:
	buffer_inv sc1
.Lgb_spin_6:
	global_load_dword v11, v6, s[100:101] sc1
	v_add_u32_e32 v10, 1, v10
	s_waitcnt vmcnt(0)
	v_cmp_ge_u32_e32 vcc, v11, v9
	s_cbranch_vccnz .Lgb_done_6
	v_cmp_gt_u32_e32 vcc, 0x80000, v10
	s_sleep 1
	s_cbranch_vccnz .Lgb_spin_6

.LBB0_1151:
	s_cmp_gt_i32 s81, 7
	s_cselect_b64 s[4:5], -1, 0
	s_and_b64 s[0:1], s[76:77], s[4:5]
	v_readlane_b32 s86, v253, 40
	s_andn2_b64 vcc, exec, s[0:1]
	v_readlane_b32 s76, v253, 62
	v_readlane_b32 s77, v253, 63
	v_readlane_b32 s87, v253, 41
	s_cbranch_vccnz .LBB0_1205
	s_waitcnt vmcnt(0)
	s_waitcnt vmcnt(0) lgkmcnt(0)
	s_barrier
	s_and_saveexec_b64 s[0:1], s[78:79]
	s_cbranch_execz .LBB0_1204
	v_mov_b32_e32 v3, 1
	v_mov_b32_e32 v4, s99
	v_and_b32_e32 v5, 0xffff, v4
	v_mov_b32_e32 v1, 0x22160
	global_atomic_add v7, v5, v3, s[100:101] sc0
	ds_read_b32 v2, v1
	v_lshrrev_b32_e32 v6, 16, v4
	v_lshrrev_b32_e32 v8, 8, v5
	v_sub_u32_e32 v8, s98, v8
	v_add_u32_e32 v8, 7, v8
	v_lshrrev_b32_e32 v8, 3, v8
	v_mov_b32_e32 v9, s98
	v_min_u32_e32 v9, 8, v9
	v_mov_b32_e32 v10, 0
	s_waitcnt lgkmcnt(0)
	v_add_u32_e32 v2, 1, v2
	ds_write_b32 v1, v2
	v_mul_lo_u32 v8, v8, v2
	v_mul_lo_u32 v9, v9, v2
	s_waitcnt vmcnt(0)
	v_add_u32_e32 v7, 1, v7
	v_cmp_eq_u32_e32 vcc, v7, v8
	s_cbranch_vccz .Lgb_poll_7
	v_mov_b32_e32 v4, 0
	global_atomic_add v4, v3, s[100:101] offset:2048
	global_atomic_add v4, v3, s[100:101] offset:2304
	global_atomic_add v4, v3, s[100:101] offset:2560
	global_atomic_add v4, v3, s[100:101] offset:2816
	global_atomic_add v4, v3, s[100:101] offset:3072
	global_atomic_add v4, v3, s[100:101] offset:3328
	global_atomic_add v4, v3, s[100:101] offset:3584
	global_atomic_add v4, v3, s[100:101] offset:3840
.Lgb_poll_7:
	buffer_inv sc1
.Lgb_spin_7:
	global_load_dword v11, v6, s[100:101] sc1
	v_add_u32_e32 v10, 1, v10
	s_waitcnt vmcnt(0)
	v_cmp_ge_u32_e32 vcc, v11, v9
	s_cbranch_vccnz .Lgb_done_7
	v_cmp_gt_u32_e32 vcc, 0x80000, v10
	s_sleep 1
	s_cbranch_vccnz .Lgb_spin_7

.LBB0_1220:
	s_cmp_gt_i32 s81, 8
	s_cselect_b64 s[14:15], -1, 0
	s_and_b64 s[4:5], s[12:13], s[14:15]
	s_andn2_b64 vcc, exec, s[4:5]
	s_cbranch_vccnz .LBB0_1274
	s_waitcnt vmcnt(0)
	s_waitcnt vmcnt(0) lgkmcnt(0)
	s_barrier
	s_and_saveexec_b64 s[4:5], s[78:79]
	s_cbranch_execz .LBB0_1273
	v_mov_b32_e32 v3, 1
	v_mov_b32_e32 v4, s99
	v_and_b32_e32 v5, 0xffff, v4
	v_mov_b32_e32 v1, 0x22160
	global_atomic_add v7, v5, v3, s[100:101] sc0
	ds_read_b32 v2, v1
	v_lshrrev_b32_e32 v6, 16, v4
	v_lshrrev_b32_e32 v8, 8, v5
	v_sub_u32_e32 v8, s98, v8
	v_add_u32_e32 v8, 7, v8
	v_lshrrev_b32_e32 v8, 3, v8
	v_mov_b32_e32 v9, s98
	v_min_u32_e32 v9, 8, v9
	v_mov_b32_e32 v10, 0
	s_waitcnt lgkmcnt(0)
	v_add_u32_e32 v2, 1, v2
	ds_write_b32 v1, v2
	v_mul_lo_u32 v8, v8, v2
	v_mul_lo_u32 v9, v9, v2
	s_waitcnt vmcnt(0)
	v_add_u32_e32 v7, 1, v7
	v_cmp_eq_u32_e32 vcc, v7, v8
	s_cbranch_vccz .Lgb_poll_8
	v_mov_b32_e32 v4, 0
	global_atomic_add v4, v3, s[100:101] offset:2048
	global_atomic_add v4, v3, s[100:101] offset:2304
	global_atomic_add v4, v3, s[100:101] offset:2560
	global_atomic_add v4, v3, s[100:101] offset:2816
	global_atomic_add v4, v3, s[100:101] offset:3072
	global_atomic_add v4, v3, s[100:101] offset:3328
	global_atomic_add v4, v3, s[100:101] offset:3584
	global_atomic_add v4, v3, s[100:101] offset:3840
.Lgb_poll_8:
	buffer_inv sc1
.Lgb_spin_8:
	global_load_dword v11, v6, s[100:101] sc1
	v_add_u32_e32 v10, 1, v10
	s_waitcnt vmcnt(0)
	v_cmp_ge_u32_e32 vcc, v11, v9
	s_cbranch_vccnz .Lgb_done_8
	v_cmp_gt_u32_e32 vcc, 0x80000, v10
	s_sleep 1
	s_cbranch_vccnz .Lgb_spin_8

.LBB0_1606:
	s_cmp_gt_i32 s81, 10
	s_cselect_b64 s[0:1], -1, 0
	s_and_b64 s[4:5], s[12:13], s[0:1]
	s_andn2_b64 vcc, exec, s[4:5]
	s_waitcnt vmcnt(0)
	v_and_b32_e32 v82, 63, v0
	s_cbranch_vccnz .LBB0_1660
	s_waitcnt vmcnt(0)
	s_waitcnt lgkmcnt(0)
	s_barrier
	s_and_saveexec_b64 s[4:5], s[78:79]
	s_cbranch_execz .LBB0_1659
	v_mov_b32_e32 v3, 1
	v_mov_b32_e32 v4, s99
	v_and_b32_e32 v5, 0xffff, v4
	v_mov_b32_e32 v1, 0x22160
	global_atomic_add v7, v5, v3, s[100:101] sc0
	ds_read_b32 v2, v1
	v_lshrrev_b32_e32 v6, 16, v4
	v_lshrrev_b32_e32 v8, 8, v5
	v_sub_u32_e32 v8, s98, v8
	v_add_u32_e32 v8, 7, v8
	v_lshrrev_b32_e32 v8, 3, v8
	v_mov_b32_e32 v9, s98
	v_min_u32_e32 v9, 8, v9
	v_mov_b32_e32 v10, 0
	s_waitcnt lgkmcnt(0)
	v_add_u32_e32 v2, 1, v2
	ds_write_b32 v1, v2
	v_mul_lo_u32 v8, v8, v2
	v_mul_lo_u32 v9, v9, v2
	s_waitcnt vmcnt(0)
	v_add_u32_e32 v7, 1, v7
	v_cmp_eq_u32_e32 vcc, v7, v8
	s_cbranch_vccz .Lgb_poll_9
	v_mov_b32_e32 v4, 0
	global_atomic_add v4, v3, s[100:101] offset:2048
	global_atomic_add v4, v3, s[100:101] offset:2304
	global_atomic_add v4, v3, s[100:101] offset:2560
	global_atomic_add v4, v3, s[100:101] offset:2816
	global_atomic_add v4, v3, s[100:101] offset:3072
	global_atomic_add v4, v3, s[100:101] offset:3328
	global_atomic_add v4, v3, s[100:101] offset:3584
	global_atomic_add v4, v3, s[100:101] offset:3840
.Lgb_poll_9:
	buffer_inv sc1
.Lgb_spin_9:
	global_load_dword v11, v6, s[100:101] sc1
	v_add_u32_e32 v10, 1, v10
	s_waitcnt vmcnt(0)
	v_cmp_ge_u32_e32 vcc, v11, v9
	s_cbranch_vccnz .Lgb_done_9
	v_cmp_gt_u32_e32 vcc, 0x80000, v10
	s_sleep 1
	s_cbranch_vccnz .Lgb_spin_9

.LBB0_1750:
	s_waitcnt vmcnt(0)
	s_waitcnt lgkmcnt(0)
	s_barrier
	s_mov_b64 s[6:7], exec
	v_readlane_b32 s40, v253, 46
	s_and_b64 s[8:9], s[6:7], s[78:79]
	v_readlane_b32 s41, v253, 47
	v_readlane_b32 s42, v253, 48
	v_readlane_b32 s43, v253, 49
	v_readlane_b32 s44, v253, 50
	v_readlane_b32 s45, v253, 51
	v_readlane_b32 s52, v253, 58
	v_readlane_b32 s53, v253, 59
	v_readlane_b32 s54, v253, 60
	v_readlane_b32 s55, v253, 61
	v_and_b32_e32 v82, 63, v0
	v_readlane_b32 s46, v253, 52
	v_readlane_b32 s47, v253, 53
	v_readlane_b32 s48, v253, 54
	v_readlane_b32 s49, v253, 55
	v_readlane_b32 s50, v253, 56
	v_readlane_b32 s51, v253, 57
	s_mov_b64 exec, s[8:9]
	s_cbranch_execz .LBB0_1802
	v_mov_b32_e32 v4, 1
	v_mov_b32_e32 v5, s99
	v_and_b32_e32 v6, 0xffff, v5
	v_mov_b32_e32 v2, 0x22160
	global_atomic_add v8, v6, v4, s[100:101] sc0
	ds_read_b32 v3, v2
	v_lshrrev_b32_e32 v7, 16, v5
	v_lshrrev_b32_e32 v9, 8, v6
	v_sub_u32_e32 v9, s98, v9
	v_add_u32_e32 v9, 7, v9
	v_lshrrev_b32_e32 v9, 3, v9
	v_mov_b32_e32 v10, s98
	v_min_u32_e32 v10, 8, v10
	v_mov_b32_e32 v11, 0
	s_waitcnt lgkmcnt(0)
	v_add_u32_e32 v3, 1, v3
	ds_write_b32 v2, v3
	v_mul_lo_u32 v9, v9, v3
	v_mul_lo_u32 v10, v10, v3
	s_waitcnt vmcnt(0)
	v_add_u32_e32 v8, 1, v8
	v_cmp_eq_u32_e32 vcc, v8, v9
	s_cbranch_vccz .Lgb_poll_10
	v_mov_b32_e32 v5, 0
	global_atomic_add v5, v4, s[100:101] offset:2048
	global_atomic_add v5, v4, s[100:101] offset:2304
	global_atomic_add v5, v4, s[100:101] offset:2560
	global_atomic_add v5, v4, s[100:101] offset:2816
	global_atomic_add v5, v4, s[100:101] offset:3072
	global_atomic_add v5, v4, s[100:101] offset:3328
	global_atomic_add v5, v4, s[100:101] offset:3584
	global_atomic_add v5, v4, s[100:101] offset:3840
.Lgb_poll_10:
	buffer_inv sc1
.Lgb_spin_10:
	global_load_dword v12, v7, s[100:101] sc1
	v_add_u32_e32 v11, 1, v11
	s_waitcnt vmcnt(0)
	v_cmp_ge_u32_e32 vcc, v12, v10
	s_cbranch_vccnz .Lgb_done_10
	v_cmp_gt_u32_e32 vcc, 0x80000, v11
	s_sleep 1
	s_cbranch_vccnz .Lgb_spin_10

.LBB0_1811:
	s_cmp_gt_i32 s81, 11
	s_cselect_b64 s[4:5], -1, 0
	s_and_b64 s[0:1], s[0:1], s[4:5]
	v_readlane_b32 s36, v253, 46
	s_andn2_b64 vcc, exec, s[0:1]
	v_readlane_b32 s37, v253, 47
	v_readlane_b32 s38, v253, 48
	v_readlane_b32 s39, v253, 49
	v_readlane_b32 s40, v253, 50
	v_readlane_b32 s41, v253, 51
	v_readlane_b32 s48, v253, 58
	v_readlane_b32 s49, v253, 59
	v_readlane_b32 s50, v253, 60
	v_readlane_b32 s51, v253, 61
	v_readlane_b32 s42, v253, 52
	v_readlane_b32 s43, v253, 53
	v_readlane_b32 s44, v253, 54
	v_readlane_b32 s45, v253, 55
	v_readlane_b32 s46, v253, 56
	v_readlane_b32 s47, v253, 57
	s_cbranch_vccnz .LBB0_1865
	s_waitcnt vmcnt(0)
	s_waitcnt lgkmcnt(0)
	s_barrier
	s_and_saveexec_b64 s[0:1], s[78:79]
	s_cbranch_execz .LBB0_1864
	v_mov_b32_e32 v3, 1
	v_mov_b32_e32 v4, s99
	v_and_b32_e32 v5, 0xffff, v4
	v_mov_b32_e32 v1, 0x22160
	global_atomic_add v7, v5, v3, s[100:101] sc0
	ds_read_b32 v2, v1
	v_lshrrev_b32_e32 v6, 16, v4
	v_lshrrev_b32_e32 v8, 8, v5
	v_sub_u32_e32 v8, s98, v8
	v_add_u32_e32 v8, 7, v8
	v_lshrrev_b32_e32 v8, 3, v8
	v_mov_b32_e32 v9, s98
	v_min_u32_e32 v9, 8, v9
	v_mov_b32_e32 v10, 0
	s_waitcnt lgkmcnt(0)
	v_add_u32_e32 v2, 1, v2
	ds_write_b32 v1, v2
	v_mul_lo_u32 v8, v8, v2
	v_mul_lo_u32 v9, v9, v2
	s_waitcnt vmcnt(0)
	v_add_u32_e32 v7, 1, v7
	v_cmp_eq_u32_e32 vcc, v7, v8
	s_cbranch_vccz .Lgb_poll_11
	v_mov_b32_e32 v4, 0
	global_atomic_add v4, v3, s[100:101] offset:2048
	global_atomic_add v4, v3, s[100:101] offset:2304
	global_atomic_add v4, v3, s[100:101] offset:2560
	global_atomic_add v4, v3, s[100:101] offset:2816
	global_atomic_add v4, v3, s[100:101] offset:3072
	global_atomic_add v4, v3, s[100:101] offset:3328
	global_atomic_add v4, v3, s[100:101] offset:3584
	global_atomic_add v4, v3, s[100:101] offset:3840
.Lgb_poll_11:
	buffer_inv sc1
.Lgb_spin_11:
	global_load_dword v11, v6, s[100:101] sc1
	v_add_u32_e32 v10, 1, v10
	s_waitcnt vmcnt(0)
	v_cmp_ge_u32_e32 vcc, v11, v9
	s_cbranch_vccnz .Lgb_done_11
	v_cmp_gt_u32_e32 vcc, 0x80000, v10
	s_sleep 1
	s_cbranch_vccnz .Lgb_spin_11

.LBB0_1890:
	s_cmp_gt_i32 s81, 12
	s_cselect_b64 s[2:3], -1, 0
	s_and_b64 s[0:1], s[0:1], s[2:3]
	s_andn2_b64 vcc, exec, s[0:1]
	s_cbranch_vccnz .LBB0_1944
	s_waitcnt vmcnt(0)
	s_waitcnt lgkmcnt(0)
	s_barrier
	s_and_saveexec_b64 s[0:1], s[78:79]
	s_cbranch_execz .LBB0_1943
	v_mov_b32_e32 v3, 1
	v_mov_b32_e32 v4, s99
	v_and_b32_e32 v5, 0xffff, v4
	v_mov_b32_e32 v1, 0x22160
	global_atomic_add v7, v5, v3, s[100:101] sc0
	ds_read_b32 v2, v1
	v_lshrrev_b32_e32 v6, 16, v4
	v_lshrrev_b32_e32 v8, 8, v5
	v_sub_u32_e32 v8, s98, v8
	v_add_u32_e32 v8, 7, v8
	v_lshrrev_b32_e32 v8, 3, v8
	v_mov_b32_e32 v9, s98
	v_min_u32_e32 v9, 8, v9
	v_mov_b32_e32 v10, 0
	s_waitcnt lgkmcnt(0)
	v_add_u32_e32 v2, 1, v2
	ds_write_b32 v1, v2
	v_mul_lo_u32 v8, v8, v2
	v_mul_lo_u32 v9, v9, v2
	s_waitcnt vmcnt(0)
	v_add_u32_e32 v7, 1, v7
	v_cmp_eq_u32_e32 vcc, v7, v8
	s_cbranch_vccz .Lgb_poll_12
	v_mov_b32_e32 v4, 0
	global_atomic_add v4, v3, s[100:101] offset:2048
	global_atomic_add v4, v3, s[100:101] offset:2304
	global_atomic_add v4, v3, s[100:101] offset:2560
	global_atomic_add v4, v3, s[100:101] offset:2816
	global_atomic_add v4, v3, s[100:101] offset:3072
	global_atomic_add v4, v3, s[100:101] offset:3328
	global_atomic_add v4, v3, s[100:101] offset:3584
	global_atomic_add v4, v3, s[100:101] offset:3840
.Lgb_poll_12:
	buffer_inv sc1
.Lgb_spin_12:
	global_load_dword v11, v6, s[100:101] sc1
	v_add_u32_e32 v10, 1, v10
	s_waitcnt vmcnt(0)
	v_cmp_ge_u32_e32 vcc, v11, v9
	s_cbranch_vccnz .Lgb_done_12
	v_cmp_gt_u32_e32 vcc, 0x80000, v10
	s_sleep 1
	s_cbranch_vccnz .Lgb_spin_12

.LBB0_1991:
	s_cmp_gt_i32 s81, 13
	s_cselect_b64 s[2:3], -1, 0
	s_and_b64 s[0:1], s[0:1], s[2:3]
	s_andn2_b64 vcc, exec, s[0:1]
	s_cbranch_vccnz .LBB0_2045
	s_waitcnt vmcnt(0)
	s_waitcnt lgkmcnt(0)
	s_barrier
	s_and_saveexec_b64 s[0:1], s[78:79]
	s_cbranch_execz .LBB0_2044
	v_mov_b32_e32 v3, 1
	v_mov_b32_e32 v4, s99
	v_and_b32_e32 v5, 0xffff, v4
	v_mov_b32_e32 v1, 0x22160
	global_atomic_add v7, v5, v3, s[100:101] sc0
	ds_read_b32 v2, v1
	v_lshrrev_b32_e32 v6, 16, v4
	v_lshrrev_b32_e32 v8, 8, v5
	v_sub_u32_e32 v8, s98, v8
	v_add_u32_e32 v8, 7, v8
	v_lshrrev_b32_e32 v8, 3, v8
	v_mov_b32_e32 v9, s98
	v_min_u32_e32 v9, 8, v9
	v_mov_b32_e32 v10, 0
	s_waitcnt lgkmcnt(0)
	v_add_u32_e32 v2, 1, v2
	ds_write_b32 v1, v2
	v_mul_lo_u32 v8, v8, v2
	v_mul_lo_u32 v9, v9, v2
	s_waitcnt vmcnt(0)
	v_add_u32_e32 v7, 1, v7
	v_cmp_eq_u32_e32 vcc, v7, v8
	s_cbranch_vccz .Lgb_poll_13
	v_mov_b32_e32 v4, 0
	global_atomic_add v4, v3, s[100:101] offset:2048
	global_atomic_add v4, v3, s[100:101] offset:2304
	global_atomic_add v4, v3, s[100:101] offset:2560
	global_atomic_add v4, v3, s[100:101] offset:2816
	global_atomic_add v4, v3, s[100:101] offset:3072
	global_atomic_add v4, v3, s[100:101] offset:3328
	global_atomic_add v4, v3, s[100:101] offset:3584
	global_atomic_add v4, v3, s[100:101] offset:3840
.Lgb_poll_13:
	buffer_inv sc1
.Lgb_spin_13:
	global_load_dword v11, v6, s[100:101] sc1
	v_add_u32_e32 v10, 1, v10
	s_waitcnt vmcnt(0)
	v_cmp_ge_u32_e32 vcc, v11, v9
	s_cbranch_vccnz .Lgb_done_13
	v_cmp_gt_u32_e32 vcc, 0x80000, v10
	s_sleep 1
	s_cbranch_vccnz .Lgb_spin_13
